# PEER V gather: expert-range test evaluated once per 16-row batch (batch-uniform) instead of per entry; 180 SALU removed, MFMA hazard distances kept
# speedup vs baseline: 1.0209x; 1.0050x over previous
.Lpv_skip1:
	s_lshl_b32 s30, s56, 4
	s_cmp_ge_i32 s30, s60
	s_cselect_b64 s[38:39], -1, 0
	s_cmp_lt_i32 s30, s48
	s_cselect_b64 s[52:53], -1, 0
	s_waitcnt lgkmcnt(0)
	v_mul_f32_e32 v1, 0x45000000, v170
	s_and_b64 vcc, s[38:39], s[52:53]
	v_cndmask_b32_e32 v1, 0, v1, vcc
	v_mov_b32_e32 v2, v0
	v_cvt_pk_fp8_f32 v2, v1, v1
	v_mul_f32_e32 v169, 0x45000000, v171
	v_cvt_pk_fp8_f32 v2, v1, v1 op_sel:[0,0,1]
	v_cndmask_b32_e32 v169, 0, v169, vcc
	v_mov_b32_e32 v170, v0
	v_cvt_pk_fp8_f32 v170, v169, v169
	v_mov_b32_e32 v3, v0
	v_and_b32_e32 v2, v2, v249
	v_cvt_pk_fp8_f32 v170, v169, v169 op_sel:[0,0,1]
	v_mul_f32_e32 v169, 0x45000000, v172
	v_mov_b32_e32 v1, v2
	v_mfma_f32_16x16x32_fp8_fp8 v[160:163], v[2:3], v[68:69], v[160:163]
	v_cndmask_b32_e32 v169, 0, v169, vcc
	v_mfma_f32_16x16x32_fp8_fp8 v[152:155], v[2:3], v[70:71], v[152:155]
	v_and_b32_e32 v2, v170, v249
	v_mov_b32_e32 v170, v0
	v_cvt_pk_fp8_f32 v170, v169, v169
	v_mfma_f32_16x16x32_fp8_fp8 v[164:167], v[0:1], v[68:69], v[164:167]
	v_cvt_pk_fp8_f32 v170, v169, v169 op_sel:[0,0,1]
	v_mfma_f32_16x16x32_fp8_fp8 v[156:159], v[0:1], v[70:71], v[156:159]
	v_mov_b32_e32 v1, v2
	v_mfma_f32_16x16x32_fp8_fp8 v[160:163], v[2:3], v[72:73], v[160:163]
	v_mfma_f32_16x16x32_fp8_fp8 v[152:155], v[2:3], v[74:75], v[152:155]
	v_and_b32_e32 v2, v170, v249
	v_mov_b32_e32 v170, v0
	s_nop 0
	v_mfma_f32_16x16x32_fp8_fp8 v[184:187], v[2:3], v[76:77], v[160:163]
	s_nop 1
	s_nop 1
	v_mul_f32_e32 v160, 0x45000000, v173
	v_cndmask_b32_e32 v169, 0, v160, vcc
	v_cvt_pk_fp8_f32 v170, v169, v169
	v_mfma_f32_16x16x32_fp8_fp8 v[164:167], v[0:1], v[72:73], v[164:167]
	v_cvt_pk_fp8_f32 v170, v169, v169 op_sel:[0,0,1]
	v_mfma_f32_16x16x32_fp8_fp8 v[156:159], v[0:1], v[74:75], v[156:159]
	v_mov_b32_e32 v1, v2
	v_mfma_f32_16x16x32_fp8_fp8 v[160:163], v[2:3], v[78:79], v[152:155]
	v_and_b32_e32 v2, v170, v249
	ds_read_b128 v[170:173], v168 offset:16
	v_mfma_f32_16x16x32_fp8_fp8 v[164:167], v[0:1], v[76:77], v[164:167]
	s_waitcnt lgkmcnt(0)
	v_mul_f32_e32 v169, 0x45000000, v170
	v_cndmask_b32_e32 v169, 0, v169, vcc
	v_mov_b32_e32 v170, v0
	v_cvt_pk_fp8_f32 v170, v169, v169
	v_mfma_f32_16x16x32_fp8_fp8 v[156:159], v[0:1], v[78:79], v[156:159]
	v_mov_b32_e32 v1, v2
	v_cvt_pk_fp8_f32 v170, v169, v169 op_sel:[0,0,1]
	v_mul_f32_e32 v169, 0x45000000, v171
	v_mfma_f32_16x16x32_fp8_fp8 v[152:155], v[2:3], v[80:81], v[184:187]
	v_cndmask_b32_e32 v169, 0, v169, vcc
	v_mfma_f32_16x16x32_fp8_fp8 v[160:163], v[2:3], v[82:83], v[160:163]
	v_and_b32_e32 v2, v170, v249
	v_mov_b32_e32 v170, v0
	v_cvt_pk_fp8_f32 v170, v169, v169
	v_cvt_pk_fp8_f32 v170, v169, v169 op_sel:[0,0,1]
	v_mul_f32_e32 v169, 0x45000000, v172
	v_mfma_f32_16x16x32_fp8_fp8 v[164:167], v[0:1], v[80:81], v[164:167]
	v_cndmask_b32_e32 v169, 0, v169, vcc
	v_mfma_f32_16x16x32_fp8_fp8 v[156:159], v[0:1], v[82:83], v[156:159]
	v_mov_b32_e32 v1, v2
	v_mfma_f32_16x16x32_fp8_fp8 v[152:155], v[2:3], v[84:85], v[152:155]
	v_mfma_f32_16x16x32_fp8_fp8 v[160:163], v[2:3], v[86:87], v[160:163]
	v_and_b32_e32 v2, v170, v249
	v_mov_b32_e32 v170, v0
	v_cvt_pk_fp8_f32 v170, v169, v169
	v_mfma_f32_16x16x32_fp8_fp8 v[164:167], v[0:1], v[84:85], v[164:167]
	v_cvt_pk_fp8_f32 v170, v169, v169 op_sel:[0,0,1]
	v_mul_f32_e32 v169, 0x45000000, v173
	v_mfma_f32_16x16x32_fp8_fp8 v[156:159], v[0:1], v[86:87], v[156:159]
	v_mov_b32_e32 v1, v2
	v_cndmask_b32_e32 v169, 0, v169, vcc
	v_mfma_f32_16x16x32_fp8_fp8 v[152:155], v[2:3], v[88:89], v[152:155]
	v_mfma_f32_16x16x32_fp8_fp8 v[160:163], v[2:3], v[90:91], v[160:163]
	v_and_b32_e32 v2, v170, v249
	v_mov_b32_e32 v170, v0
	v_cvt_pk_fp8_f32 v170, v169, v169
	v_mfma_f32_16x16x32_fp8_fp8 v[164:167], v[0:1], v[88:89], v[164:167]
	v_cvt_pk_fp8_f32 v170, v169, v169 op_sel:[0,0,1]
	v_mfma_f32_16x16x32_fp8_fp8 v[156:159], v[0:1], v[90:91], v[156:159]
	v_mov_b32_e32 v1, v2
	v_mfma_f32_16x16x32_fp8_fp8 v[152:155], v[2:3], v[92:93], v[152:155]
	v_mfma_f32_16x16x32_fp8_fp8 v[160:163], v[2:3], v[94:95], v[160:163]
	v_and_b32_e32 v2, v170, v249
	ds_read_b128 v[170:173], v168 offset:32
	s_waitcnt lgkmcnt(0)
	v_mul_f32_e32 v169, 0x45000000, v170
	v_cndmask_b32_e32 v169, 0, v169, vcc
	v_mov_b32_e32 v170, v0
	v_cvt_pk_fp8_f32 v170, v169, v169
	v_mfma_f32_16x16x32_fp8_fp8 v[164:167], v[0:1], v[92:93], v[164:167]
	v_cvt_pk_fp8_f32 v170, v169, v169 op_sel:[0,0,1]
	v_mul_f32_e32 v169, 0x45000000, v171
	v_mfma_f32_16x16x32_fp8_fp8 v[156:159], v[0:1], v[94:95], v[156:159]
	v_mov_b32_e32 v1, v2
	v_cndmask_b32_e32 v169, 0, v169, vcc
	v_mfma_f32_16x16x32_fp8_fp8 v[152:155], v[2:3], v[96:97], v[152:155]
	v_mfma_f32_16x16x32_fp8_fp8 v[160:163], v[2:3], v[98:99], v[160:163]
	v_and_b32_e32 v2, v170, v249
	v_mov_b32_e32 v170, v0
	v_cvt_pk_fp8_f32 v170, v169, v169
	v_mfma_f32_16x16x32_fp8_fp8 v[164:167], v[0:1], v[96:97], v[164:167]
	v_cvt_pk_fp8_f32 v170, v169, v169 op_sel:[0,0,1]
	v_mul_f32_e32 v169, 0x45000000, v172
	v_mfma_f32_16x16x32_fp8_fp8 v[156:159], v[0:1], v[98:99], v[156:159]
	v_mov_b32_e32 v1, v2
	v_cndmask_b32_e32 v169, 0, v169, vcc
	v_mfma_f32_16x16x32_fp8_fp8 v[152:155], v[2:3], v[100:101], v[152:155]
	v_mfma_f32_16x16x32_fp8_fp8 v[160:163], v[2:3], v[102:103], v[160:163]
	v_and_b32_e32 v2, v170, v249
	v_mov_b32_e32 v170, v0
	v_cvt_pk_fp8_f32 v170, v169, v169
	v_mfma_f32_16x16x32_fp8_fp8 v[164:167], v[0:1], v[100:101], v[164:167]
	v_cvt_pk_fp8_f32 v170, v169, v169 op_sel:[0,0,1]
	v_mul_f32_e32 v169, 0x45000000, v173
	v_mfma_f32_16x16x32_fp8_fp8 v[156:159], v[0:1], v[102:103], v[156:159]
	v_mov_b32_e32 v1, v2
	v_cndmask_b32_e32 v169, 0, v169, vcc
	v_mfma_f32_16x16x32_fp8_fp8 v[152:155], v[2:3], v[104:105], v[152:155]
	v_mfma_f32_16x16x32_fp8_fp8 v[160:163], v[2:3], v[106:107], v[160:163]
	v_and_b32_e32 v2, v170, v249
	v_mov_b32_e32 v170, v0
	v_cvt_pk_fp8_f32 v170, v169, v169
	v_mfma_f32_16x16x32_fp8_fp8 v[164:167], v[0:1], v[104:105], v[164:167]
	v_mov_b32_e32 v172, v0
	v_cvt_pk_fp8_f32 v170, v169, v169 op_sel:[0,0,1]
	v_mfma_f32_16x16x32_fp8_fp8 v[156:159], v[0:1], v[106:107], v[156:159]
	v_mov_b32_e32 v1, v2
	v_mfma_f32_16x16x32_fp8_fp8 v[152:155], v[2:3], v[108:109], v[152:155]
	v_mfma_f32_16x16x32_fp8_fp8 v[160:163], v[2:3], v[110:111], v[160:163]
	v_and_b32_e32 v2, v170, v249
	ds_read_b128 v[168:171], v168 offset:48
	v_mov_b32_e32 v173, v0
	v_mfma_f32_16x16x32_fp8_fp8 v[164:167], v[0:1], v[108:109], v[164:167]
	s_waitcnt lgkmcnt(0)
	v_mul_f32_e32 v168, 0x45000000, v168
	v_cndmask_b32_e32 v168, 0, v168, vcc
	v_cvt_pk_fp8_f32 v172, v168, v168
	v_mfma_f32_16x16x32_fp8_fp8 v[156:159], v[0:1], v[110:111], v[156:159]
	v_mov_b32_e32 v1, v2
	v_cvt_pk_fp8_f32 v172, v168, v168 op_sel:[0,0,1]
	v_mul_f32_e32 v168, 0x45000000, v169
	v_cndmask_b32_e32 v168, 0, v168, vcc
	v_mov_b32_e32 v169, v0
	v_cvt_pk_fp8_f32 v169, v168, v168
	v_mfma_f32_16x16x32_fp8_fp8 v[152:155], v[2:3], v[112:113], v[152:155]
	v_cvt_pk_fp8_f32 v169, v168, v168 op_sel:[0,0,1]
	v_mfma_f32_16x16x32_fp8_fp8 v[160:163], v[2:3], v[114:115], v[160:163]
	v_and_b32_e32 v2, v172, v249
	v_mul_f32_e32 v168, 0x45000000, v170
	v_mfma_f32_16x16x32_fp8_fp8 v[164:167], v[0:1], v[112:113], v[164:167]
	v_cndmask_b32_e32 v168, 0, v168, vcc
	v_mfma_f32_16x16x32_fp8_fp8 v[156:159], v[0:1], v[114:115], v[156:159]
	v_mov_b32_e32 v1, v2
	v_mfma_f32_16x16x32_fp8_fp8 v[152:155], v[2:3], v[120:121], v[152:155]
	s_add_i32 s30, s61, -1
	v_mfma_f32_16x16x32_fp8_fp8 v[160:163], v[2:3], v[122:123], v[160:163]
	v_and_b32_e32 v2, v169, v249
	v_mov_b32_e32 v169, v0
	v_cvt_pk_fp8_f32 v169, v168, v168
	v_mfma_f32_16x16x32_fp8_fp8 v[164:167], v[0:1], v[120:121], v[164:167]
	s_cmp_lg_u32 s56, s30
	v_cvt_pk_fp8_f32 v169, v168, v168 op_sel:[0,0,1]
	v_mul_f32_e32 v168, 0x45000000, v171
	v_mfma_f32_16x16x32_fp8_fp8 v[156:159], v[0:1], v[122:123], v[156:159]
	v_mov_b32_e32 v1, v2
	v_cndmask_b32_e32 v172, 0, v168, vcc
	v_cvt_pk_fp8_f32 v173, v172, v172
	v_mfma_f32_16x16x32_fp8_fp8 v[152:155], v[2:3], v[124:125], v[152:155]
	v_cvt_pk_fp8_f32 v173, v172, v172 op_sel:[0,0,1]
	v_mfma_f32_16x16x32_fp8_fp8 v[160:163], v[2:3], v[126:127], v[160:163]
	v_and_b32_e32 v2, v169, v249
	v_mfma_f32_16x16x32_fp8_fp8 v[164:167], v[0:1], v[124:125], v[164:167]
	v_mfma_f32_16x16x32_fp8_fp8 v[156:159], v[0:1], v[126:127], v[156:159]
	v_mov_b32_e32 v1, v2
	v_mfma_f32_16x16x32_fp8_fp8 v[152:155], v[2:3], v[144:145], v[152:155]
	v_mfma_f32_16x16x32_fp8_fp8 v[168:171], v[2:3], v[146:147], v[160:163]
	v_and_b32_e32 v2, v173, v249
	v_mfma_f32_16x16x32_fp8_fp8 v[164:167], v[0:1], v[144:145], v[164:167]
	v_mfma_f32_16x16x32_fp8_fp8 v[156:159], v[0:1], v[146:147], v[156:159]
	v_mov_b32_e32 v1, v2
	s_nop 0
	v_mfma_f32_16x16x32_fp8_fp8 v[160:163], v[2:3], v[148:149], v[152:155]
	v_mfma_f32_16x16x32_fp8_fp8 v[164:167], v[0:1], v[148:149], v[164:167]
	v_mfma_f32_16x16x32_fp8_fp8 v[152:155], v[2:3], v[150:151], v[168:171]
	v_mfma_f32_16x16x32_fp8_fp8 v[156:159], v[0:1], v[150:151], v[156:159]
	s_cbranch_scc1 .LBB0_1816
	v_cvt_pk_f32_fp8_e32 v[2:3], v140
	v_cvt_pk_f32_fp8_e32 v[170:171], v141
	v_cvt_pk_f32_fp8_sdwa v[172:173], v141 src0_sel:WORD_1
	v_cvt_pk_f32_fp8_sdwa v[188:189], v142 src0_sel:WORD_1
	v_pk_mul_f32 v[2:3], v[2:3], s[12:13] op_sel_hi:[1,0]
	v_cvt_pk_f32_fp8_e32 v[186:187], v142
	v_pk_fma_f32 v[174:175], v[160:161], s[14:15], v[2:3] op_sel_hi:[1,0,1]
	v_pk_mul_f32 v[2:3], v[170:171], s[12:13] op_sel_hi:[1,0]
	v_pk_mul_f32 v[170:171], v[172:173], s[12:13] op_sel_hi:[1,0]
	v_cvt_pk_f32_fp8_sdwa v[168:169], v140 src0_sel:WORD_1
	v_pk_fma_f32 v[172:173], v[166:167], s[14:15], v[170:171] op_sel_hi:[1,0,1]
	v_pk_mul_f32 v[170:171], v[188:189], s[12:13] op_sel_hi:[1,0]
	v_cvt_pk_f32_fp8_e32 v[188:189], v143
	v_cvt_pk_f32_fp8_sdwa v[192:193], v143 src0_sel:WORD_1
	s_ashr_i32 s30, s58, 31
	s_add_u32 s52, s0, s58
	v_pk_fma_f32 v[184:185], v[164:165], s[14:15], v[2:3] op_sel_hi:[1,0,1]
	v_pk_mul_f32 v[2:3], v[186:187], s[12:13] op_sel_hi:[1,0]
	s_addc_u32 s53, s1, s30
	v_pk_mul_f32 v[168:169], v[168:169], s[12:13] op_sel_hi:[1,0]
	v_pk_fma_f32 v[186:187], v[154:155], s[14:15], v[170:171] op_sel_hi:[1,0,1]
	v_pk_fma_f32 v[190:191], v[152:153], s[14:15], v[2:3] op_sel_hi:[1,0,1]
	v_pk_mul_f32 v[2:3], v[188:189], s[12:13] op_sel_hi:[1,0]
	v_pk_mul_f32 v[170:171], v[192:193], s[12:13] op_sel_hi:[1,0]
	s_lshl_b64 s[38:39], s[52:53], 10
	v_pk_fma_f32 v[168:169], v[162:163], s[14:15], v[168:169] op_sel_hi:[1,0,1]
	v_pk_fma_f32 v[188:189], v[158:159], s[14:15], v[170:171] op_sel_hi:[1,0,1]
	v_pk_fma_f32 v[192:193], v[156:157], s[14:15], v[2:3] op_sel_hi:[1,0,1]
	s_andn2_b64 vcc, exec, s[46:47]
	s_mov_b64 s[54:55], -1
	s_cbranch_vccnz .LBB0_1811
	v_pk_mul_f32 v[2:3], v[174:175], s[8:9] op_sel_hi:[1,0]
	v_mov_b32_e32 v194, v0
	v_cvt_pk_fp8_f32 v194, v2, v3
	v_pk_mul_f32 v[2:3], v[184:185], s[8:9] op_sel_hi:[1,0]
	v_mov_b32_e32 v195, v0
	v_cvt_pk_fp8_f32 v195, v2, v3
	v_pk_mul_f32 v[2:3], v[168:169], s[8:9] op_sel_hi:[1,0]
	v_mov_b32_e32 v196, v0
	v_cvt_pk_fp8_f32 v194, v2, v3 op_sel:[0,0,1]
	v_pk_mul_f32 v[2:3], v[172:173], s[8:9] op_sel_hi:[1,0]
	v_mov_b32_e32 v197, v0
	v_cvt_pk_fp8_f32 v195, v2, v3 op_sel:[0,0,1]
	v_pk_mul_f32 v[2:3], v[190:191], s[8:9] op_sel_hi:[1,0]
	s_mov_b64 s[54:55], 0
	v_cvt_pk_fp8_f32 v196, v2, v3
	v_pk_mul_f32 v[2:3], v[192:193], s[8:9] op_sel_hi:[1,0]
	s_nop 0
	v_cvt_pk_fp8_f32 v197, v2, v3
	v_pk_mul_f32 v[2:3], v[186:187], s[8:9] op_sel_hi:[1,0]
	s_nop 0
	v_cvt_pk_fp8_f32 v196, v2, v3 op_sel:[0,0,1]
	v_pk_mul_f32 v[2:3], v[188:189], s[8:9] op_sel_hi:[1,0]
	s_nop 0
	v_cvt_pk_fp8_f32 v197, v2, v3 op_sel:[0,0,1]
	v_lshl_add_u64 v[2:3], v[234:235], 0, s[38:39]
	global_store_dwordx4 v[2:3], v[194:197], off

.LBB0_1842:
	s_and_b64 s[38:39], s[6:7], exec
	s_cselect_b32 s52, s61, 0x80
	s_and_b64 s[38:39], s[40:41], exec
	s_cselect_b32 s52, s60, s52
	s_and_b64 s[38:39], s[42:43], exec
	s_cselect_b32 s39, s48, s52
	s_lshl_b32 s52, s57, 9
	s_add_i32 s52, s15, s52
	s_lshl_b32 s53, s59, 6
	s_add_i32 s52, s52, s53
	v_mov_b32_e32 v176, s52
	s_lshr_b32 s38, s39, 4
	s_add_i32 s70, s70, 1
	ds_read_b128 v[178:181], v176
	s_max_u32 s38, s38, s70
	s_lshl_b32 s48, s59, 4
	s_cmp_ge_i32 s48, s30
	s_cselect_b64 s[52:53], -1, 0
	s_cmp_lt_i32 s48, s39
	s_cselect_b64 s[54:55], -1, 0
	s_waitcnt lgkmcnt(0)
	v_mul_f32_e32 v1, 0x45000000, v178
	s_and_b64 vcc, s[52:53], s[54:55]
	v_cndmask_b32_e32 v1, 0, v1, vcc
	v_mov_b32_e32 v2, v0
	v_cvt_pk_fp8_f32 v2, v1, v1
	v_mul_f32_e32 v177, 0x45000000, v179
	v_cvt_pk_fp8_f32 v2, v1, v1 op_sel:[0,0,1]
	v_cndmask_b32_e32 v177, 0, v177, vcc
	v_mov_b32_e32 v178, v0
	v_cvt_pk_fp8_f32 v178, v177, v177
	v_and_b32_e32 v2, v2, v249
	v_mov_b32_e32 v3, v0
	v_cvt_pk_fp8_f32 v178, v177, v177 op_sel:[0,0,1]
	v_mul_f32_e32 v177, 0x45000000, v180
	v_mfma_f32_16x16x32_fp8_fp8 v[160:163], v[2:3], v[4:5], v[160:163]
	v_mov_b32_e32 v1, v2
	v_cndmask_b32_e32 v177, 0, v177, vcc
	v_mfma_f32_16x16x32_fp8_fp8 v[152:155], v[2:3], v[6:7], v[152:155]
	v_and_b32_e32 v2, v178, v249
	v_mov_b32_e32 v178, v0
	v_cvt_pk_fp8_f32 v178, v177, v177
	v_mfma_f32_16x16x32_fp8_fp8 v[164:167], v[0:1], v[4:5], v[164:167]
	v_cvt_pk_fp8_f32 v178, v177, v177 op_sel:[0,0,1]
	v_mfma_f32_16x16x32_fp8_fp8 v[156:159], v[0:1], v[6:7], v[156:159]
	v_mov_b32_e32 v1, v2
	v_mfma_f32_16x16x32_fp8_fp8 v[160:163], v[2:3], v[8:9], v[160:163]
	v_mfma_f32_16x16x32_fp8_fp8 v[152:155], v[2:3], v[10:11], v[152:155]
	v_and_b32_e32 v2, v178, v249
	v_mov_b32_e32 v178, v0
	s_nop 0
	v_mfma_f32_16x16x32_fp8_fp8 v[182:185], v[2:3], v[12:13], v[160:163]
	s_nop 1
	s_nop 1
	v_mul_f32_e32 v160, 0x45000000, v181
	v_cndmask_b32_e32 v177, 0, v160, vcc
	v_cvt_pk_fp8_f32 v178, v177, v177
	v_mfma_f32_16x16x32_fp8_fp8 v[164:167], v[0:1], v[8:9], v[164:167]
	v_cvt_pk_fp8_f32 v178, v177, v177 op_sel:[0,0,1]
	v_mfma_f32_16x16x32_fp8_fp8 v[156:159], v[0:1], v[10:11], v[156:159]
	v_mov_b32_e32 v1, v2
	v_mfma_f32_16x16x32_fp8_fp8 v[160:163], v[2:3], v[14:15], v[152:155]
	v_and_b32_e32 v2, v178, v249
	ds_read_b128 v[178:181], v176 offset:16
	v_mfma_f32_16x16x32_fp8_fp8 v[164:167], v[0:1], v[12:13], v[164:167]
	s_waitcnt lgkmcnt(0)
	v_mul_f32_e32 v177, 0x45000000, v178
	v_cndmask_b32_e32 v177, 0, v177, vcc
	v_mov_b32_e32 v178, v0
	v_cvt_pk_fp8_f32 v178, v177, v177
	v_mfma_f32_16x16x32_fp8_fp8 v[156:159], v[0:1], v[14:15], v[156:159]
	v_mov_b32_e32 v1, v2
	v_cvt_pk_fp8_f32 v178, v177, v177 op_sel:[0,0,1]
	v_mul_f32_e32 v177, 0x45000000, v179
	v_mfma_f32_16x16x32_fp8_fp8 v[152:155], v[2:3], v[16:17], v[182:185]
	v_cndmask_b32_e32 v177, 0, v177, vcc
	v_mfma_f32_16x16x32_fp8_fp8 v[160:163], v[2:3], v[18:19], v[160:163]
	v_and_b32_e32 v2, v178, v249
	v_mov_b32_e32 v178, v0
	v_cvt_pk_fp8_f32 v178, v177, v177
	v_cvt_pk_fp8_f32 v178, v177, v177 op_sel:[0,0,1]
	v_mul_f32_e32 v177, 0x45000000, v180
	v_mfma_f32_16x16x32_fp8_fp8 v[164:167], v[0:1], v[16:17], v[164:167]
	v_cndmask_b32_e32 v177, 0, v177, vcc
	v_mfma_f32_16x16x32_fp8_fp8 v[156:159], v[0:1], v[18:19], v[156:159]
	v_mov_b32_e32 v1, v2
	v_mfma_f32_16x16x32_fp8_fp8 v[152:155], v[2:3], v[20:21], v[152:155]
	v_mfma_f32_16x16x32_fp8_fp8 v[160:163], v[2:3], v[22:23], v[160:163]
	v_and_b32_e32 v2, v178, v249
	v_mov_b32_e32 v178, v0
	v_cvt_pk_fp8_f32 v178, v177, v177
	v_mfma_f32_16x16x32_fp8_fp8 v[164:167], v[0:1], v[20:21], v[164:167]
	v_cvt_pk_fp8_f32 v178, v177, v177 op_sel:[0,0,1]
	v_mul_f32_e32 v177, 0x45000000, v181
	v_mfma_f32_16x16x32_fp8_fp8 v[156:159], v[0:1], v[22:23], v[156:159]
	v_mov_b32_e32 v1, v2
	v_cndmask_b32_e32 v177, 0, v177, vcc
	v_mfma_f32_16x16x32_fp8_fp8 v[152:155], v[2:3], v[24:25], v[152:155]
	v_mfma_f32_16x16x32_fp8_fp8 v[160:163], v[2:3], v[26:27], v[160:163]
	v_and_b32_e32 v2, v178, v249
	v_mov_b32_e32 v178, v0
	v_cvt_pk_fp8_f32 v178, v177, v177
	v_mfma_f32_16x16x32_fp8_fp8 v[164:167], v[0:1], v[24:25], v[164:167]
	v_cvt_pk_fp8_f32 v178, v177, v177 op_sel:[0,0,1]
	v_mfma_f32_16x16x32_fp8_fp8 v[156:159], v[0:1], v[26:27], v[156:159]
	v_mov_b32_e32 v1, v2
	v_mfma_f32_16x16x32_fp8_fp8 v[152:155], v[2:3], v[28:29], v[152:155]
	v_mfma_f32_16x16x32_fp8_fp8 v[160:163], v[2:3], v[30:31], v[160:163]
	v_and_b32_e32 v2, v178, v249
	ds_read_b128 v[178:181], v176 offset:32
	s_waitcnt lgkmcnt(0)
	v_mul_f32_e32 v177, 0x45000000, v178
	v_cndmask_b32_e32 v177, 0, v177, vcc
	v_mov_b32_e32 v178, v0
	v_cvt_pk_fp8_f32 v178, v177, v177
	v_mfma_f32_16x16x32_fp8_fp8 v[164:167], v[0:1], v[28:29], v[164:167]
	v_cvt_pk_fp8_f32 v178, v177, v177 op_sel:[0,0,1]
	v_mul_f32_e32 v177, 0x45000000, v179
	v_mfma_f32_16x16x32_fp8_fp8 v[156:159], v[0:1], v[30:31], v[156:159]
	v_mov_b32_e32 v1, v2
	v_cndmask_b32_e32 v177, 0, v177, vcc
	v_mfma_f32_16x16x32_fp8_fp8 v[152:155], v[2:3], v[32:33], v[152:155]
	v_mfma_f32_16x16x32_fp8_fp8 v[160:163], v[2:3], v[34:35], v[160:163]
	v_and_b32_e32 v2, v178, v249
	v_mov_b32_e32 v178, v0
	v_cvt_pk_fp8_f32 v178, v177, v177
	v_mfma_f32_16x16x32_fp8_fp8 v[164:167], v[0:1], v[32:33], v[164:167]
	v_cvt_pk_fp8_f32 v178, v177, v177 op_sel:[0,0,1]
	v_mul_f32_e32 v177, 0x45000000, v180
	v_mfma_f32_16x16x32_fp8_fp8 v[156:159], v[0:1], v[34:35], v[156:159]
	v_mov_b32_e32 v1, v2
	v_cndmask_b32_e32 v177, 0, v177, vcc
	v_mfma_f32_16x16x32_fp8_fp8 v[152:155], v[2:3], v[36:37], v[152:155]
	v_mfma_f32_16x16x32_fp8_fp8 v[160:163], v[2:3], v[38:39], v[160:163]
	v_and_b32_e32 v2, v178, v249
	v_mov_b32_e32 v178, v0
	v_cvt_pk_fp8_f32 v178, v177, v177
	v_mfma_f32_16x16x32_fp8_fp8 v[164:167], v[0:1], v[36:37], v[164:167]
	v_cvt_pk_fp8_f32 v178, v177, v177 op_sel:[0,0,1]
	v_mul_f32_e32 v177, 0x45000000, v181
	v_mfma_f32_16x16x32_fp8_fp8 v[156:159], v[0:1], v[38:39], v[156:159]
	v_mov_b32_e32 v1, v2
	v_cndmask_b32_e32 v177, 0, v177, vcc
	v_mfma_f32_16x16x32_fp8_fp8 v[152:155], v[2:3], v[40:41], v[152:155]
	v_mfma_f32_16x16x32_fp8_fp8 v[160:163], v[2:3], v[42:43], v[160:163]
	v_and_b32_e32 v2, v178, v249
	v_mov_b32_e32 v178, v0
	v_cvt_pk_fp8_f32 v178, v177, v177
	v_mfma_f32_16x16x32_fp8_fp8 v[164:167], v[0:1], v[40:41], v[164:167]
	v_mov_b32_e32 v180, v0
	v_cvt_pk_fp8_f32 v178, v177, v177 op_sel:[0,0,1]
	v_mfma_f32_16x16x32_fp8_fp8 v[156:159], v[0:1], v[42:43], v[156:159]
	v_mov_b32_e32 v1, v2
	v_mfma_f32_16x16x32_fp8_fp8 v[152:155], v[2:3], v[44:45], v[152:155]
	v_mfma_f32_16x16x32_fp8_fp8 v[160:163], v[2:3], v[46:47], v[160:163]
	v_and_b32_e32 v2, v178, v249
	ds_read_b128 v[176:179], v176 offset:48
	v_mov_b32_e32 v181, v0
	v_mfma_f32_16x16x32_fp8_fp8 v[164:167], v[0:1], v[44:45], v[164:167]
	s_waitcnt lgkmcnt(0)
; __device__ __forceinline__ void peer_token_end(Frame& F, const Args& a, int layer, bool last, bool final_half, size_t tok, int lane, const f32x2 (&out)[8], const f32x4 (&hpre)[4], const v4u (&gpre)[2], const v4u& p8pre) {
;     ...
;     for (int i = 0; i < 4; ++i) { const f32x2 lo = __builtin_amdgcn_cvt_pk_f32_fp8((int)p8pre[i], false), hi = __builtin_amdgcn_cvt_pk_f32_fp8((int)p8pre[i], true);
;         pe[i] = (f32x4){lo.x, lo.y, hi.x, hi.y} * (1.f / 256.f) + (f32x4){out[2 * i].x, out[2 * i].y, out[2 * i + 1].x, out[2 * i + 1].y}; }
;     if (!final_half) {
;         v4u w;
; #pragma unroll
;         for (int i = 0; i < 4; ++i) { const f32x4 s8 = pe[i] * 256.f; int t = 0; t = __builtin_amdgcn_cvt_pk_fp8_f32(s8.x, s8.y, t, false); t = __builtin_amdgcn_cvt_pk_fp8_f32(s8.z, s8.w, t, true); w[i] = (unsigned)t; }
;         *(v4u*)((unsigned char*)(F.ws + WS_P8) + tok * 1024 + 16 * lane) = w;
	v_mul_f32_e32 v176, 0x45000000, v176
	v_cndmask_b32_e32 v176, 0, v176, vcc
	v_cvt_pk_fp8_f32 v180, v176, v176
	v_mfma_f32_16x16x32_fp8_fp8 v[156:159], v[0:1], v[46:47], v[156:159]
	v_mov_b32_e32 v1, v2
	v_cvt_pk_fp8_f32 v180, v176, v176 op_sel:[0,0,1]
	v_mul_f32_e32 v176, 0x45000000, v177
	v_cndmask_b32_e32 v176, 0, v176, vcc
	v_mov_b32_e32 v177, v0
	v_cvt_pk_fp8_f32 v177, v176, v176
	v_mfma_f32_16x16x32_fp8_fp8 v[152:155], v[2:3], v[48:49], v[152:155]
	v_cvt_pk_fp8_f32 v177, v176, v176 op_sel:[0,0,1]
	v_mfma_f32_16x16x32_fp8_fp8 v[160:163], v[2:3], v[50:51], v[160:163]
	v_and_b32_e32 v2, v180, v249
	v_mul_f32_e32 v176, 0x45000000, v178
	v_mfma_f32_16x16x32_fp8_fp8 v[164:167], v[0:1], v[48:49], v[164:167]
	v_cndmask_b32_e32 v176, 0, v176, vcc
	v_mfma_f32_16x16x32_fp8_fp8 v[156:159], v[0:1], v[50:51], v[156:159]
	v_mov_b32_e32 v1, v2
	v_mfma_f32_16x16x32_fp8_fp8 v[152:155], v[2:3], v[52:53], v[152:155]
	s_add_i32 s38, s38, -1
	v_mfma_f32_16x16x32_fp8_fp8 v[160:163], v[2:3], v[54:55], v[160:163]
	v_and_b32_e32 v2, v177, v249
	v_mov_b32_e32 v177, v0
	v_cvt_pk_fp8_f32 v177, v176, v176
	v_mfma_f32_16x16x32_fp8_fp8 v[164:167], v[0:1], v[52:53], v[164:167]
	s_cmp_lg_u32 s59, s38
	v_cvt_pk_fp8_f32 v177, v176, v176 op_sel:[0,0,1]
	v_mul_f32_e32 v176, 0x45000000, v179
	v_mfma_f32_16x16x32_fp8_fp8 v[156:159], v[0:1], v[54:55], v[156:159]
	v_mov_b32_e32 v1, v2
	v_cndmask_b32_e32 v180, 0, v176, vcc
	v_cvt_pk_fp8_f32 v181, v180, v180
	v_mfma_f32_16x16x32_fp8_fp8 v[152:155], v[2:3], v[56:57], v[152:155]
	v_cvt_pk_fp8_f32 v181, v180, v180 op_sel:[0,0,1]
	v_mfma_f32_16x16x32_fp8_fp8 v[160:163], v[2:3], v[58:59], v[160:163]
	v_and_b32_e32 v2, v177, v249
	v_mfma_f32_16x16x32_fp8_fp8 v[164:167], v[0:1], v[56:57], v[164:167]
	v_mfma_f32_16x16x32_fp8_fp8 v[156:159], v[0:1], v[58:59], v[156:159]
	v_mov_b32_e32 v1, v2
	v_mfma_f32_16x16x32_fp8_fp8 v[152:155], v[2:3], v[60:61], v[152:155]
	v_mfma_f32_16x16x32_fp8_fp8 v[176:179], v[2:3], v[62:63], v[160:163]
	v_and_b32_e32 v2, v181, v249
	v_mfma_f32_16x16x32_fp8_fp8 v[164:167], v[0:1], v[60:61], v[164:167]
	v_mfma_f32_16x16x32_fp8_fp8 v[156:159], v[0:1], v[62:63], v[156:159]
	v_mov_b32_e32 v1, v2
	v_mfma_f32_16x16x32_fp8_fp8 v[160:163], v[2:3], v[64:65], v[152:155]
	s_nop 0
	v_mfma_f32_16x16x32_fp8_fp8 v[164:167], v[0:1], v[64:65], v[164:167]
	v_mfma_f32_16x16x32_fp8_fp8 v[152:155], v[2:3], v[66:67], v[176:179]
	v_mfma_f32_16x16x32_fp8_fp8 v[156:159], v[0:1], v[66:67], v[156:159]
	s_cbranch_scc1 .LBB0_1850
	s_waitcnt vmcnt(0)
	v_cvt_pk_f32_fp8_e32 v[2:3], v140
	v_cvt_pk_f32_fp8_e32 v[178:179], v141
	v_cvt_pk_f32_fp8_sdwa v[180:181], v141 src0_sel:WORD_1
	v_cvt_pk_f32_fp8_sdwa v[188:189], v142 src0_sel:WORD_1
	v_pk_mul_f32 v[2:3], v[2:3], s[12:13] op_sel_hi:[1,0]
	v_cvt_pk_f32_fp8_e32 v[186:187], v142
	v_pk_fma_f32 v[182:183], v[160:161], s[14:15], v[2:3] op_sel_hi:[1,0,1]
	v_pk_mul_f32 v[2:3], v[178:179], s[12:13] op_sel_hi:[1,0]
	v_pk_mul_f32 v[178:179], v[180:181], s[12:13] op_sel_hi:[1,0]
	v_cvt_pk_f32_fp8_sdwa v[176:177], v140 src0_sel:WORD_1
	v_pk_fma_f32 v[180:181], v[166:167], s[14:15], v[178:179] op_sel_hi:[1,0,1]
	v_pk_mul_f32 v[178:179], v[188:189], s[12:13] op_sel_hi:[1,0]
	v_cvt_pk_f32_fp8_e32 v[188:189], v143
	v_cvt_pk_f32_fp8_sdwa v[192:193], v143 src0_sel:WORD_1
	s_ashr_i32 s30, s57, 31
	s_add_u32 s52, s0, s57
	v_pk_fma_f32 v[184:185], v[164:165], s[14:15], v[2:3] op_sel_hi:[1,0,1]
	v_pk_mul_f32 v[2:3], v[186:187], s[12:13] op_sel_hi:[1,0]
	s_addc_u32 s53, s1, s30
	v_pk_mul_f32 v[176:177], v[176:177], s[12:13] op_sel_hi:[1,0]
	v_pk_fma_f32 v[186:187], v[154:155], s[14:15], v[178:179] op_sel_hi:[1,0,1]
	v_pk_fma_f32 v[190:191], v[152:153], s[14:15], v[2:3] op_sel_hi:[1,0,1]
	v_pk_mul_f32 v[2:3], v[188:189], s[12:13] op_sel_hi:[1,0]
	v_pk_mul_f32 v[178:179], v[192:193], s[12:13] op_sel_hi:[1,0]
	s_lshl_b64 s[38:39], s[52:53], 10
	v_pk_fma_f32 v[176:177], v[162:163], s[14:15], v[176:177] op_sel_hi:[1,0,1]
	v_pk_fma_f32 v[188:189], v[158:159], s[14:15], v[178:179] op_sel_hi:[1,0,1]
	v_pk_fma_f32 v[192:193], v[156:157], s[14:15], v[2:3] op_sel_hi:[1,0,1]
	s_andn2_b64 vcc, exec, s[46:47]
	s_mov_b64 s[54:55], -1
	s_cbranch_vccnz .LBB0_1845
	v_pk_mul_f32 v[2:3], v[182:183], s[8:9] op_sel_hi:[1,0]
	v_mov_b32_e32 v194, v0
	v_cvt_pk_fp8_f32 v194, v2, v3
	v_pk_mul_f32 v[2:3], v[184:185], s[8:9] op_sel_hi:[1,0]
	v_mov_b32_e32 v195, v0
	v_cvt_pk_fp8_f32 v195, v2, v3
	v_pk_mul_f32 v[2:3], v[176:177], s[8:9] op_sel_hi:[1,0]
	v_mov_b32_e32 v196, v0
	v_cvt_pk_fp8_f32 v194, v2, v3 op_sel:[0,0,1]
	v_pk_mul_f32 v[2:3], v[180:181], s[8:9] op_sel_hi:[1,0]
	v_mov_b32_e32 v197, v0
	v_cvt_pk_fp8_f32 v195, v2, v3 op_sel:[0,0,1]
	v_pk_mul_f32 v[2:3], v[190:191], s[8:9] op_sel_hi:[1,0]
	s_mov_b64 s[54:55], 0
	v_cvt_pk_fp8_f32 v196, v2, v3
	v_pk_mul_f32 v[2:3], v[192:193], s[8:9] op_sel_hi:[1,0]
	s_nop 0
	v_cvt_pk_fp8_f32 v197, v2, v3
	v_pk_mul_f32 v[2:3], v[186:187], s[8:9] op_sel_hi:[1,0]
	s_nop 0
	v_cvt_pk_fp8_f32 v196, v2, v3 op_sel:[0,0,1]
	v_pk_mul_f32 v[2:3], v[188:189], s[8:9] op_sel_hi:[1,0]
	s_nop 0
	v_cvt_pk_fp8_f32 v197, v2, v3 op_sel:[0,0,1]
	v_lshl_add_u64 v[2:3], v[234:235], 0, s[38:39]
	global_store_dwordx4 v[2:3], v[194:197], off
